# speedup vs baseline: 1.0234x; 1.0022x over previous
_Z11gemm_kernelILi256ELi192ELi4ELi2ELi4ELi2ELi2ELi0EEvPKDF16_S1_iiiPDF16_PfPK15HIP_vector_typeIfLj2EE:
	s_load_dwordx8 s[4:11], s[0:1], 0x0
	s_load_dwordx2 s[12:13], s[0:1], 0x30
	s_lshr_b32 s18, s2, 3
	v_readfirstlane_b32 s17, v0
	s_lshr_b32 s14, s17, 6
	s_waitcnt lgkmcnt(0)
	s_ashr_i32 s11, s8, 31
	s_lshr_b32 s3, s11, 22
	s_add_i32 s3, s8, s3
	s_ashr_i32 s15, s3, 10
	s_abs_i32 s16, s15
	v_cvt_f32_u32_e32 v1, s16
	s_sub_i32 s21, 0, s16
	s_mul_hi_i32 s19, s9, 0x2aaaaaab
	s_lshr_b32 s20, s19, 31
	v_rcp_iflag_f32_e32 v1, v1
	s_ashr_i32 s19, s19, 6
	s_add_i32 s19, s19, s20
	s_bfe_u32 s20, s2, 0x20001
	v_mul_f32_e32 v1, 0x4f7ffffe, v1
	v_cvt_u32_f32_e32 v1, v1
	s_ashr_i32 s3, s3, 31
	s_mul_i32 s20, s15, s20
	v_mov_b32_e32 v97, 0
	v_readfirstlane_b32 s22, v1
	s_mul_i32 s21, s21, s22
	s_mul_hi_u32 s21, s22, s21
	s_add_i32 s22, s22, s21
	s_mul_hi_u32 s22, s18, s22
	s_mul_i32 s21, s22, s16
	s_sub_i32 s23, s18, s21
	s_add_i32 s24, s22, 1
	s_sub_i32 s25, s23, s16
	s_cmp_ge_u32 s23, s16
	s_cselect_b32 s22, s24, s22
	s_cselect_b32 s23, s25, s23
	s_add_i32 s24, s22, 1
	s_cmp_ge_u32 s23, s16
	s_cselect_b32 s16, s24, s22
	s_xor_b32 s16, s16, s3
	s_sub_i32 s3, s16, s3
	s_mul_i32 s15, s3, s15
	s_sub_i32 s15, s18, s15
	s_add_i32 s15, s15, s20
	s_bitcmp1_b32 s2, 0
	v_bfe_u32 v1, v0, 3, 3
	s_cselect_b32 s2, s19, 0
	v_lshl_or_b32 v1, s14, 3, v1
	s_add_i32 s18, s3, s2
	s_lshl_b32 s19, s15, 8
	v_lshrrev_b32_e32 v2, 1, v1
	s_lshl_b32 s2, s14, 10
	v_xor_b32_e32 v6, v2, v0
	v_add_u32_e32 v2, s19, v1
	s_cmp_lg_u32 0, -1
	s_mul_i32 s15, s18, 0xc0
	v_ashrrev_i32_e32 v3, 31, v2
	s_cselect_b32 s3, 0, 0
	v_lshlrev_b64 v[2:3], 7, v[2:3]
	v_add_u32_e32 v4, s15, v1
	s_add_i32 s22, s2, s3
	v_lshlrev_b32_e32 v1, 4, v6
	s_lshr_b32 s3, s17, 1
	v_lshl_add_u64 v[2:3], s[4:5], 0, v[2:3]
	v_ashrrev_i32_e32 v5, 31, v4
	v_and_b32_e32 v96, 0x70, v1
	s_add_i32 s24, s22, 0x8000
	s_and_b32 s20, s3, 0x7fffffc0
	v_lshlrev_b64 v[4:5], 7, v[4:5]
	v_lshl_add_u64 v[104:105], v[2:3], 0, v[96:97]
	s_bitcmp1_b32 s17, 6
	s_mov_b64 s[4:5], 0x2000
	s_mov_b32 m0, s22
	s_nop 0
	global_load_lds_dwordx4 v[104:105], off
	v_lshl_add_u64 v[4:5], s[6:7], 0, v[4:5]
	s_cselect_b32 s16, 0x60, 0
	v_lshl_add_u64 v[110:111], v[104:105], 0, s[4:5]
	s_mov_b64 s[6:7], 0x4000
	s_add_i32 s3, s22, 0x2000
	s_mov_b32 m0, s3
	s_nop 0
	global_load_lds_dwordx4 v[110:111], off
	v_lshl_add_u64 v[108:109], v[104:105], 0, s[6:7]
	s_mov_b64 s[26:27], 0x6000
	s_add_i32 s3, s22, 0x4000
	s_mov_b32 m0, s3
	s_nop 0
	global_load_lds_dwordx4 v[108:109], off
	v_lshl_add_u64 v[106:107], v[104:105], 0, s[26:27]
	s_add_i32 s3, s22, 0x6000
	s_mov_b32 m0, s3
	s_nop 0
	global_load_lds_dwordx4 v[106:107], off
	v_lshl_add_u64 v[98:99], v[4:5], 0, v[96:97]
	s_mov_b32 m0, s24
	s_nop 0
	global_load_lds_dwordx4 v[98:99], off
	v_lshl_add_u64 v[100:101], v[98:99], 0, s[4:5]
	s_add_i32 s3, s22, 0xa000
	s_mov_b32 m0, s3
	s_nop 0
	global_load_lds_dwordx4 v[100:101], off
	v_lshl_add_u64 v[102:103], v[98:99], 0, s[6:7]
	s_add_i32 s3, s22, 0xc000
	s_mov_b32 m0, s3
	s_nop 0
	global_load_lds_dwordx4 v[102:103], off
	s_mov_b32 s21, 1
	s_mov_b32 s23, 0
	s_cmp_lt_i32 s10, 64
	v_mov_b32_e32 v96, v97
	v_mov_b32_e32 v95, v97
	v_mov_b32_e32 v94, v97
	v_mov_b32_e32 v93, v97
	v_mov_b32_e32 v92, v97
	v_mov_b32_e32 v91, v97
	v_mov_b32_e32 v90, v97
	v_mov_b32_e32 v89, v97
	v_mov_b32_e32 v88, v97
	v_mov_b32_e32 v87, v97
	v_mov_b32_e32 v86, v97
	v_mov_b32_e32 v85, v97
	v_mov_b32_e32 v84, v97
	v_mov_b32_e32 v83, v97
	v_mov_b32_e32 v82, v97
	v_mov_b32_e32 v81, v97
	v_mov_b32_e32 v80, v97
	v_mov_b32_e32 v79, v97
	v_mov_b32_e32 v78, v97
	v_mov_b32_e32 v77, v97
	v_mov_b32_e32 v76, v97
	v_mov_b32_e32 v75, v97
	v_mov_b32_e32 v74, v97
	v_mov_b32_e32 v73, v97
	v_mov_b32_e32 v72, v97
	v_mov_b32_e32 v71, v97
	v_mov_b32_e32 v70, v97
	v_mov_b32_e32 v69, v97
	v_mov_b32_e32 v68, v97
	v_mov_b32_e32 v67, v97
	v_mov_b32_e32 v66, v97
	v_mov_b32_e32 v65, v97
	v_mov_b32_e32 v64, v97
	v_mov_b32_e32 v63, v97
	v_mov_b32_e32 v62, v97
	v_mov_b32_e32 v61, v97
	v_mov_b32_e32 v60, v97
	v_mov_b32_e32 v59, v97
	v_mov_b32_e32 v58, v97
	v_mov_b32_e32 v57, v97
	v_mov_b32_e32 v56, v97
	v_mov_b32_e32 v55, v97
	v_mov_b32_e32 v54, v97
	v_mov_b32_e32 v53, v97
	v_mov_b32_e32 v52, v97
	v_mov_b32_e32 v51, v97
	v_mov_b32_e32 v50, v97
	v_mov_b32_e32 v49, v97
	v_mov_b32_e32 v48, v97
	v_mov_b32_e32 v47, v97
	v_mov_b32_e32 v46, v97
	v_mov_b32_e32 v45, v97
	v_mov_b32_e32 v44, v97
	v_mov_b32_e32 v43, v97
	v_mov_b32_e32 v42, v97
	v_mov_b32_e32 v41, v97
	v_mov_b32_e32 v40, v97
	v_mov_b32_e32 v39, v97
	v_mov_b32_e32 v38, v97
	v_mov_b32_e32 v37, v97
	v_mov_b32_e32 v36, v97
	v_mov_b32_e32 v35, v97
	v_mov_b32_e32 v34, v97
	v_mov_b32_e32 v33, v97
	v_mov_b32_e32 v32, v97
	v_mov_b32_e32 v31, v97
	v_mov_b32_e32 v30, v97
	v_mov_b32_e32 v29, v97
	v_mov_b32_e32 v28, v97
	v_mov_b32_e32 v27, v97
	v_mov_b32_e32 v26, v97
	v_mov_b32_e32 v25, v97
	v_mov_b32_e32 v24, v97
	v_mov_b32_e32 v23, v97
	v_mov_b32_e32 v22, v97
	v_mov_b32_e32 v21, v97
	v_mov_b32_e32 v20, v97
	v_mov_b32_e32 v19, v97
	v_mov_b32_e32 v18, v97
	v_mov_b32_e32 v17, v97
	v_mov_b32_e32 v16, v97
	v_mov_b32_e32 v15, v97
	v_mov_b32_e32 v14, v97
	v_mov_b32_e32 v13, v97
	v_mov_b32_e32 v12, v97
	v_mov_b32_e32 v11, v97
	v_mov_b32_e32 v10, v97
	v_mov_b32_e32 v9, v97
	v_mov_b32_e32 v8, v97
	v_mov_b32_e32 v7, v97
	v_mov_b32_e32 v6, v97
	v_mov_b32_e32 v5, v97
	v_mov_b32_e32 v4, v97
	v_mov_b32_e32 v3, v97
	v_mov_b32_e32 v2, v97
	v_and_b32_e32 v162, 31, v0
	v_bfe_u32 v1, v0, 5, 1
	s_cbranch_scc1 .LBB2_6
	s_ashr_i32 s3, s10, 31
	s_lshr_b32 s3, s3, 26
	s_add_i32 s3, s10, s3
	v_lshrrev_b32_e32 v2, 1, v0
	s_ashr_i32 s25, s3, 6
	v_bitop3_b32 v2, v1, v2, 7 bitop3:0x78
	s_cmp_lg_u32 0, -1
	v_lshlrev_b32_e32 v120, 4, v2
	v_or_b32_e32 v2, s20, v162
	s_cselect_b32 s3, 0, 0
	v_lshl_add_u32 v121, v2, 7, 0
	v_or_b32_e32 v2, s16, v162
	s_mov_b32 s10, s8
	s_add_i32 s8, s3, s2
	s_ashr_i32 s3, s9, 31
	s_mov_b32 s2, s9
	v_lshl_add_u32 v122, v2, 7, 0
	s_lshl_b64 s[2:3], s[2:3], 7
	v_mov_b32_e32 v2, 0
	s_addk_i32 s8, 0x6000
	v_xor_b32_e32 v123, 32, v120
	v_xor_b32_e32 v124, 64, v120
	v_xor_b32_e32 v125, 0x60, v120
	s_lshl_b64 s[4:5], s[10:11], 7
	s_mov_b64 s[6:7], s[2:3]
	s_mov_b32 s9, 0
	v_mov_b32_e32 v3, v2
	v_mov_b32_e32 v4, v2
	v_mov_b32_e32 v5, v2
	v_mov_b32_e32 v6, v2
	v_mov_b32_e32 v7, v2
	v_mov_b32_e32 v8, v2
	v_mov_b32_e32 v9, v2
	v_mov_b32_e32 v10, v2
	v_mov_b32_e32 v11, v2
	v_mov_b32_e32 v12, v2
	v_mov_b32_e32 v13, v2
	v_mov_b32_e32 v14, v2
	v_mov_b32_e32 v15, v2
	v_mov_b32_e32 v16, v2
	v_mov_b32_e32 v17, v2
	v_mov_b32_e32 v18, v2
	v_mov_b32_e32 v19, v2
	v_mov_b32_e32 v20, v2
	v_mov_b32_e32 v21, v2
	v_mov_b32_e32 v22, v2
	v_mov_b32_e32 v23, v2
	v_mov_b32_e32 v24, v2
	v_mov_b32_e32 v25, v2
	v_mov_b32_e32 v26, v2
	v_mov_b32_e32 v27, v2
	v_mov_b32_e32 v28, v2
	v_mov_b32_e32 v29, v2
	v_mov_b32_e32 v30, v2
	v_mov_b32_e32 v31, v2
	v_mov_b32_e32 v32, v2
	v_mov_b32_e32 v33, v2
	v_mov_b32_e32 v34, v2
	v_mov_b32_e32 v35, v2
	v_mov_b32_e32 v36, v2
	v_mov_b32_e32 v37, v2
	v_mov_b32_e32 v38, v2
	v_mov_b32_e32 v39, v2
	v_mov_b32_e32 v40, v2
	v_mov_b32_e32 v41, v2
	v_mov_b32_e32 v42, v2
	v_mov_b32_e32 v43, v2
	v_mov_b32_e32 v44, v2
	v_mov_b32_e32 v45, v2
	v_mov_b32_e32 v46, v2
	v_mov_b32_e32 v47, v2
	v_mov_b32_e32 v48, v2
	v_mov_b32_e32 v49, v2
	v_mov_b32_e32 v50, v2
	v_mov_b32_e32 v51, v2
	v_mov_b32_e32 v52, v2
	v_mov_b32_e32 v53, v2
	v_mov_b32_e32 v54, v2
	v_mov_b32_e32 v55, v2
	v_mov_b32_e32 v56, v2
	v_mov_b32_e32 v57, v2
	v_mov_b32_e32 v58, v2
	v_mov_b32_e32 v59, v2
	v_mov_b32_e32 v60, v2
	v_mov_b32_e32 v61, v2
	v_mov_b32_e32 v62, v2
	v_mov_b32_e32 v63, v2
	v_mov_b32_e32 v64, v2
	v_mov_b32_e32 v65, v2
	v_mov_b32_e32 v66, v2
	v_mov_b32_e32 v67, v2
	v_mov_b32_e32 v68, v2
	v_mov_b32_e32 v69, v2
	v_mov_b32_e32 v70, v2
	v_mov_b32_e32 v71, v2
	v_mov_b32_e32 v72, v2
	v_mov_b32_e32 v73, v2
	v_mov_b32_e32 v74, v2
	v_mov_b32_e32 v75, v2
	v_mov_b32_e32 v76, v2
	v_mov_b32_e32 v77, v2
	v_mov_b32_e32 v78, v2
	v_mov_b32_e32 v79, v2
	v_mov_b32_e32 v80, v2
	v_mov_b32_e32 v81, v2
	v_mov_b32_e32 v82, v2
	v_mov_b32_e32 v83, v2
	v_mov_b32_e32 v84, v2
	v_mov_b32_e32 v85, v2
	v_mov_b32_e32 v86, v2
	v_mov_b32_e32 v87, v2
	v_mov_b32_e32 v88, v2
	v_mov_b32_e32 v89, v2
	v_mov_b32_e32 v90, v2
	v_mov_b32_e32 v91, v2
	v_mov_b32_e32 v92, v2
	v_mov_b32_e32 v93, v2
	v_mov_b32_e32 v94, v2
	v_mov_b32_e32 v95, v2
	v_mov_b32_e32 v96, v2
	v_mov_b32_e32 v97, v2
	v_lshl_add_u64 v[190:191], v[104:105], 0, s[4:5]
	v_lshl_add_u64 v[192:193], v[110:111], 0, s[4:5]
	v_lshl_add_u64 v[194:195], v[108:109], 0, s[4:5]
	v_lshl_add_u64 v[196:197], v[106:107], 0, s[4:5]
	v_lshl_add_u64 v[198:199], v[98:99], 0, s[2:3]
	v_lshl_add_u64 v[200:201], v[100:101], 0, s[2:3]
	v_lshl_add_u64 v[202:203], v[102:103], 0, s[2:3]
	v_and_b32_e32 v184, 15, v0
	v_bfe_u32 v185, v0, 4, 2
	v_lshrrev_b32_e32 v186, 1, v184
	v_xor_b32_e32 v186, v185, v186
	v_lshlrev_b32_e32 v182, 4, v186
	v_xor_b32_e32 v183, 64, v182
	v_add_u32_e32 v180, s20, v184
	v_lshlrev_b32_e32 v180, 7, v180
	v_add_u32_e32 v181, s16, v184
	v_lshlrev_b32_e32 v181, 7, v181
	v_add_u32_e32 v181, 0x8000, v181
	s_add_i32 s25, s25, -1
	s_cmp_ge_u32 s14, 4
	s_cbranch_scc1 .Lqkv_aloop
	s_waitcnt vmcnt(0)
	s_barrier
	s_mul_i32 s10, s23, 0xe000
	s_mul_i32 s11, s21, 0xe000
	v_add_u32_e32 v184, s10, v180
	v_add_u32_e32 v185, s10, v181
	s_add_i32 s11, s11, s22
	s_xor_b32 s23, s23, 1
	s_xor_b32 s21, s21, 1
	v_add_u32_e32 v186, v184, v182
	v_add_u32_e32 v187, v185, v182
	ds_read_b128 v[100:103], v186
	ds_read_b128 v[116:119], v187
	ds_read_b128 v[120:123], v187 offset:2048
	ds_read_b128 v[124:127], v187 offset:4096
	ds_read_b128 v[128:131], v187 offset:6144
	ds_read_b128 v[132:135], v187 offset:8192
	ds_read_b128 v[136:139], v187 offset:10240
	ds_read_b128 v[104:107], v186 offset:2048
	ds_read_b128 v[108:111], v186 offset:4096
	ds_read_b128 v[112:115], v186 offset:6144
	s_mov_b32 m0, s11
	s_nop 0
	global_load_lds_dwordx4 v[190:191], off
	v_lshl_add_u64 v[190:191], v[190:191], 0, s[4:5]
	s_add_i32 m0, s11, 0x2000
	s_nop 0
	global_load_lds_dwordx4 v[192:193], off
	v_lshl_add_u64 v[192:193], v[192:193], 0, s[4:5]
	s_waitcnt lgkmcnt(8)
	s_add_i32 m0, s11, 0x4000
	v_mfma_f32_16x16x32_f16 v[2:5], v[116:119], v[100:103], v[2:5]
	global_load_lds_dwordx4 v[194:195], off
	v_lshl_add_u64 v[194:195], v[194:195], 0, s[4:5]
	s_waitcnt lgkmcnt(7)
	v_mfma_f32_16x16x32_f16 v[6:9], v[120:123], v[100:103], v[6:9]
	s_waitcnt lgkmcnt(6)
	v_mfma_f32_16x16x32_f16 v[10:13], v[124:127], v[100:103], v[10:13]
	s_waitcnt lgkmcnt(5)
	v_mfma_f32_16x16x32_f16 v[14:17], v[128:131], v[100:103], v[14:17]
	s_waitcnt lgkmcnt(4)
	s_add_i32 m0, s11, 0x6000
	v_mfma_f32_16x16x32_f16 v[18:21], v[132:135], v[100:103], v[18:21]
	global_load_lds_dwordx4 v[196:197], off
	v_lshl_add_u64 v[196:197], v[196:197], 0, s[4:5]
	s_waitcnt lgkmcnt(3)
	v_mfma_f32_16x16x32_f16 v[22:25], v[136:139], v[100:103], v[22:25]
	v_add_u32_e32 v188, v184, v183
	v_add_u32_e32 v189, v185, v183
	ds_read_b128 v[140:143], v188
	ds_read_b128 v[156:159], v189
	ds_read_b128 v[160:163], v189 offset:2048
	ds_read_b128 v[164:167], v189 offset:4096
	ds_read_b128 v[168:171], v189 offset:6144
	ds_read_b128 v[172:175], v189 offset:8192
	ds_read_b128 v[176:179], v189 offset:10240
	ds_read_b128 v[144:147], v188 offset:2048
	ds_read_b128 v[148:151], v188 offset:4096
	ds_read_b128 v[152:155], v188 offset:6144
	s_waitcnt lgkmcnt(12)
	v_mfma_f32_16x16x32_f16 v[26:29], v[116:119], v[104:107], v[26:29]
	v_mfma_f32_16x16x32_f16 v[30:33], v[120:123], v[104:107], v[30:33]
	s_add_i32 m0, s11, 0x8000
	v_mfma_f32_16x16x32_f16 v[34:37], v[124:127], v[104:107], v[34:37]
	global_load_lds_dwordx4 v[198:199], off
	v_lshl_add_u64 v[198:199], v[198:199], 0, s[2:3]
	v_mfma_f32_16x16x32_f16 v[38:41], v[128:131], v[104:107], v[38:41]
	v_mfma_f32_16x16x32_f16 v[42:45], v[132:135], v[104:107], v[42:45]
	v_mfma_f32_16x16x32_f16 v[46:49], v[136:139], v[104:107], v[46:49]
	s_waitcnt lgkmcnt(11)
	s_add_i32 m0, s11, 0xa000
	v_mfma_f32_16x16x32_f16 v[50:53], v[116:119], v[108:111], v[50:53]
	global_load_lds_dwordx4 v[200:201], off
	v_lshl_add_u64 v[200:201], v[200:201], 0, s[2:3]
	v_mfma_f32_16x16x32_f16 v[54:57], v[120:123], v[108:111], v[54:57]
	v_mfma_f32_16x16x32_f16 v[58:61], v[124:127], v[108:111], v[58:61]
	v_mfma_f32_16x16x32_f16 v[62:65], v[128:131], v[108:111], v[62:65]
	s_add_i32 m0, s11, 0xc000
	v_mfma_f32_16x16x32_f16 v[66:69], v[132:135], v[108:111], v[66:69]
	global_load_lds_dwordx4 v[202:203], off
	v_lshl_add_u64 v[202:203], v[202:203], 0, s[2:3]
	v_mfma_f32_16x16x32_f16 v[70:73], v[136:139], v[108:111], v[70:73]
	s_waitcnt lgkmcnt(10)
	v_mfma_f32_16x16x32_f16 v[74:77], v[116:119], v[112:115], v[74:77]
	v_mfma_f32_16x16x32_f16 v[78:81], v[120:123], v[112:115], v[78:81]
	v_mfma_f32_16x16x32_f16 v[82:85], v[124:127], v[112:115], v[82:85]
	v_mfma_f32_16x16x32_f16 v[86:89], v[128:131], v[112:115], v[86:89]
	v_mfma_f32_16x16x32_f16 v[90:93], v[132:135], v[112:115], v[90:93]
	v_mfma_f32_16x16x32_f16 v[94:97], v[136:139], v[112:115], v[94:97]
	s_mov_b32 s9, 1
.Lqkv_rloop:
	s_waitcnt vmcnt(0) lgkmcnt(0)
	s_barrier
	s_mul_i32 s10, s23, 0xe000
	s_mul_i32 s11, s21, 0xe000
	v_add_u32_e32 v184, s10, v180
	v_add_u32_e32 v185, s10, v181
	s_add_i32 s11, s11, s22
	s_xor_b32 s23, s23, 1
	s_xor_b32 s21, s21, 1
	v_add_u32_e32 v186, v184, v182
	v_add_u32_e32 v187, v185, v182
	ds_read_b128 v[100:103], v186
	ds_read_b128 v[116:119], v187
	ds_read_b128 v[120:123], v187 offset:2048
	ds_read_b128 v[124:127], v187 offset:4096
	ds_read_b128 v[128:131], v187 offset:6144
	ds_read_b128 v[132:135], v187 offset:8192
	ds_read_b128 v[136:139], v187 offset:10240
	ds_read_b128 v[104:107], v186 offset:2048
	ds_read_b128 v[108:111], v186 offset:4096
	ds_read_b128 v[112:115], v186 offset:6144
	s_mov_b32 m0, s11
	v_mfma_f32_16x16x32_f16 v[2:5], v[156:159], v[140:143], v[2:5]
	global_load_lds_dwordx4 v[190:191], off
	v_lshl_add_u64 v[190:191], v[190:191], 0, s[4:5]
	v_mfma_f32_16x16x32_f16 v[6:9], v[160:163], v[140:143], v[6:9]
	v_mfma_f32_16x16x32_f16 v[10:13], v[164:167], v[140:143], v[10:13]
	s_add_i32 m0, s11, 0x2000
	v_mfma_f32_16x16x32_f16 v[14:17], v[168:171], v[140:143], v[14:17]
	global_load_lds_dwordx4 v[192:193], off
	v_lshl_add_u64 v[192:193], v[192:193], 0, s[4:5]
	v_mfma_f32_16x16x32_f16 v[18:21], v[172:175], v[140:143], v[18:21]
	v_mfma_f32_16x16x32_f16 v[22:25], v[176:179], v[140:143], v[22:25]
	s_add_i32 m0, s11, 0x4000
	v_mfma_f32_16x16x32_f16 v[26:29], v[156:159], v[144:147], v[26:29]
	global_load_lds_dwordx4 v[194:195], off
	v_lshl_add_u64 v[194:195], v[194:195], 0, s[4:5]
	v_mfma_f32_16x16x32_f16 v[30:33], v[160:163], v[144:147], v[30:33]
	v_mfma_f32_16x16x32_f16 v[34:37], v[164:167], v[144:147], v[34:37]
	s_add_i32 m0, s11, 0x6000
	v_mfma_f32_16x16x32_f16 v[38:41], v[168:171], v[144:147], v[38:41]
	global_load_lds_dwordx4 v[196:197], off
	v_lshl_add_u64 v[196:197], v[196:197], 0, s[4:5]
	v_mfma_f32_16x16x32_f16 v[42:45], v[172:175], v[144:147], v[42:45]
	v_mfma_f32_16x16x32_f16 v[46:49], v[176:179], v[144:147], v[46:49]
	s_add_i32 m0, s11, 0x8000
	v_mfma_f32_16x16x32_f16 v[50:53], v[156:159], v[148:151], v[50:53]
	global_load_lds_dwordx4 v[198:199], off
	v_lshl_add_u64 v[198:199], v[198:199], 0, s[2:3]
	v_mfma_f32_16x16x32_f16 v[54:57], v[160:163], v[148:151], v[54:57]
	v_mfma_f32_16x16x32_f16 v[58:61], v[164:167], v[148:151], v[58:61]
	s_add_i32 m0, s11, 0xa000
	v_mfma_f32_16x16x32_f16 v[62:65], v[168:171], v[148:151], v[62:65]
	global_load_lds_dwordx4 v[200:201], off
	v_lshl_add_u64 v[200:201], v[200:201], 0, s[2:3]
	v_mfma_f32_16x16x32_f16 v[66:69], v[172:175], v[148:151], v[66:69]
	v_mfma_f32_16x16x32_f16 v[70:73], v[176:179], v[148:151], v[70:73]
	s_add_i32 m0, s11, 0xc000
	v_mfma_f32_16x16x32_f16 v[74:77], v[156:159], v[152:155], v[74:77]
	global_load_lds_dwordx4 v[202:203], off
	v_lshl_add_u64 v[202:203], v[202:203], 0, s[2:3]
	v_mfma_f32_16x16x32_f16 v[78:81], v[160:163], v[152:155], v[78:81]
	v_mfma_f32_16x16x32_f16 v[82:85], v[164:167], v[152:155], v[82:85]
	v_mfma_f32_16x16x32_f16 v[86:89], v[168:171], v[152:155], v[86:89]
	v_mfma_f32_16x16x32_f16 v[90:93], v[172:175], v[152:155], v[90:93]
	v_mfma_f32_16x16x32_f16 v[94:97], v[176:179], v[152:155], v[94:97]
	v_add_u32_e32 v188, v184, v183
	v_add_u32_e32 v189, v185, v183
	ds_read_b128 v[140:143], v188
	ds_read_b128 v[156:159], v189
	ds_read_b128 v[160:163], v189 offset:2048
	ds_read_b128 v[164:167], v189 offset:4096
	ds_read_b128 v[168:171], v189 offset:6144
	ds_read_b128 v[172:175], v189 offset:8192
	ds_read_b128 v[176:179], v189 offset:10240
	ds_read_b128 v[144:147], v188 offset:2048
	ds_read_b128 v[148:151], v188 offset:4096
	ds_read_b128 v[152:155], v188 offset:6144
	s_waitcnt lgkmcnt(15)
	v_mfma_f32_16x16x32_f16 v[2:5], v[116:119], v[100:103], v[2:5]
	s_waitcnt lgkmcnt(15)
	v_mfma_f32_16x16x32_f16 v[6:9], v[120:123], v[100:103], v[6:9]
	s_waitcnt lgkmcnt(15)
	v_mfma_f32_16x16x32_f16 v[10:13], v[124:127], v[100:103], v[10:13]
	s_waitcnt lgkmcnt(15)
	v_mfma_f32_16x16x32_f16 v[14:17], v[128:131], v[100:103], v[14:17]
	s_waitcnt lgkmcnt(14)
	v_mfma_f32_16x16x32_f16 v[18:21], v[132:135], v[100:103], v[18:21]
	s_waitcnt lgkmcnt(13)
	v_mfma_f32_16x16x32_f16 v[22:25], v[136:139], v[100:103], v[22:25]
	s_waitcnt lgkmcnt(12)
	v_mfma_f32_16x16x32_f16 v[26:29], v[116:119], v[104:107], v[26:29]
	v_mfma_f32_16x16x32_f16 v[30:33], v[120:123], v[104:107], v[30:33]
	v_mfma_f32_16x16x32_f16 v[34:37], v[124:127], v[104:107], v[34:37]
	v_mfma_f32_16x16x32_f16 v[38:41], v[128:131], v[104:107], v[38:41]
	v_mfma_f32_16x16x32_f16 v[42:45], v[132:135], v[104:107], v[42:45]
	v_mfma_f32_16x16x32_f16 v[46:49], v[136:139], v[104:107], v[46:49]
	s_waitcnt lgkmcnt(11)
	v_mfma_f32_16x16x32_f16 v[50:53], v[116:119], v[108:111], v[50:53]
	v_mfma_f32_16x16x32_f16 v[54:57], v[120:123], v[108:111], v[54:57]
	v_mfma_f32_16x16x32_f16 v[58:61], v[124:127], v[108:111], v[58:61]
	v_mfma_f32_16x16x32_f16 v[62:65], v[128:131], v[108:111], v[62:65]
	v_mfma_f32_16x16x32_f16 v[66:69], v[132:135], v[108:111], v[66:69]
	v_mfma_f32_16x16x32_f16 v[70:73], v[136:139], v[108:111], v[70:73]
	s_waitcnt lgkmcnt(10)
	v_mfma_f32_16x16x32_f16 v[74:77], v[116:119], v[112:115], v[74:77]
	v_mfma_f32_16x16x32_f16 v[78:81], v[120:123], v[112:115], v[78:81]
	v_mfma_f32_16x16x32_f16 v[82:85], v[124:127], v[112:115], v[82:85]
	v_mfma_f32_16x16x32_f16 v[86:89], v[128:131], v[112:115], v[86:89]
	v_mfma_f32_16x16x32_f16 v[90:93], v[132:135], v[112:115], v[90:93]
	v_mfma_f32_16x16x32_f16 v[94:97], v[136:139], v[112:115], v[94:97]
	s_add_i32 s9, s9, 1
	s_cmp_lt_i32 s9, s25
	s_cbranch_scc1 .Lqkv_rloop
	s_waitcnt vmcnt(0) lgkmcnt(0)
	s_barrier
	s_mul_i32 s10, s23, 0xe000
	v_add_u32_e32 v184, s10, v180
	v_add_u32_e32 v185, s10, v181
	s_xor_b32 s23, s23, 1
	s_xor_b32 s21, s21, 1
	v_add_u32_e32 v186, v184, v182
	v_add_u32_e32 v187, v185, v182
	ds_read_b128 v[100:103], v186
	ds_read_b128 v[116:119], v187
	ds_read_b128 v[120:123], v187 offset:2048
	ds_read_b128 v[124:127], v187 offset:4096
	ds_read_b128 v[128:131], v187 offset:6144
	ds_read_b128 v[132:135], v187 offset:8192
	ds_read_b128 v[136:139], v187 offset:10240
	ds_read_b128 v[104:107], v186 offset:2048
	ds_read_b128 v[108:111], v186 offset:4096
	ds_read_b128 v[112:115], v186 offset:6144
	v_mfma_f32_16x16x32_f16 v[2:5], v[156:159], v[140:143], v[2:5]
	v_mfma_f32_16x16x32_f16 v[6:9], v[160:163], v[140:143], v[6:9]
	v_mfma_f32_16x16x32_f16 v[10:13], v[164:167], v[140:143], v[10:13]
	v_mfma_f32_16x16x32_f16 v[14:17], v[168:171], v[140:143], v[14:17]
	v_mfma_f32_16x16x32_f16 v[18:21], v[172:175], v[140:143], v[18:21]
	v_mfma_f32_16x16x32_f16 v[22:25], v[176:179], v[140:143], v[22:25]
	v_mfma_f32_16x16x32_f16 v[26:29], v[156:159], v[144:147], v[26:29]
	v_mfma_f32_16x16x32_f16 v[30:33], v[160:163], v[144:147], v[30:33]
	v_mfma_f32_16x16x32_f16 v[34:37], v[164:167], v[144:147], v[34:37]
	v_mfma_f32_16x16x32_f16 v[38:41], v[168:171], v[144:147], v[38:41]
	v_mfma_f32_16x16x32_f16 v[42:45], v[172:175], v[144:147], v[42:45]
	v_mfma_f32_16x16x32_f16 v[46:49], v[176:179], v[144:147], v[46:49]
	v_mfma_f32_16x16x32_f16 v[50:53], v[156:159], v[148:151], v[50:53]
	v_mfma_f32_16x16x32_f16 v[54:57], v[160:163], v[148:151], v[54:57]
	v_mfma_f32_16x16x32_f16 v[58:61], v[164:167], v[148:151], v[58:61]
	v_mfma_f32_16x16x32_f16 v[62:65], v[168:171], v[148:151], v[62:65]
	v_mfma_f32_16x16x32_f16 v[66:69], v[172:175], v[148:151], v[66:69]
	v_mfma_f32_16x16x32_f16 v[70:73], v[176:179], v[148:151], v[70:73]
	v_mfma_f32_16x16x32_f16 v[74:77], v[156:159], v[152:155], v[74:77]
	v_mfma_f32_16x16x32_f16 v[78:81], v[160:163], v[152:155], v[78:81]
	v_mfma_f32_16x16x32_f16 v[82:85], v[164:167], v[152:155], v[82:85]
	v_mfma_f32_16x16x32_f16 v[86:89], v[168:171], v[152:155], v[86:89]
	v_mfma_f32_16x16x32_f16 v[90:93], v[172:175], v[152:155], v[90:93]
	v_mfma_f32_16x16x32_f16 v[94:97], v[176:179], v[152:155], v[94:97]
	v_add_u32_e32 v188, v184, v183
	v_add_u32_e32 v189, v185, v183
	ds_read_b128 v[140:143], v188
	ds_read_b128 v[156:159], v189
	ds_read_b128 v[160:163], v189 offset:2048
	ds_read_b128 v[164:167], v189 offset:4096
	ds_read_b128 v[168:171], v189 offset:6144
	ds_read_b128 v[172:175], v189 offset:8192
	ds_read_b128 v[176:179], v189 offset:10240
	ds_read_b128 v[144:147], v188 offset:2048
	ds_read_b128 v[148:151], v188 offset:4096
	ds_read_b128 v[152:155], v188 offset:6144
	s_waitcnt lgkmcnt(15)
	v_mfma_f32_16x16x32_f16 v[2:5], v[116:119], v[100:103], v[2:5]
	s_waitcnt lgkmcnt(15)
	v_mfma_f32_16x16x32_f16 v[6:9], v[120:123], v[100:103], v[6:9]
	s_waitcnt lgkmcnt(15)
	v_mfma_f32_16x16x32_f16 v[10:13], v[124:127], v[100:103], v[10:13]
	s_waitcnt lgkmcnt(15)
	v_mfma_f32_16x16x32_f16 v[14:17], v[128:131], v[100:103], v[14:17]
	s_waitcnt lgkmcnt(14)
	v_mfma_f32_16x16x32_f16 v[18:21], v[132:135], v[100:103], v[18:21]
	s_waitcnt lgkmcnt(13)
	v_mfma_f32_16x16x32_f16 v[22:25], v[136:139], v[100:103], v[22:25]
	s_waitcnt lgkmcnt(12)
	v_mfma_f32_16x16x32_f16 v[26:29], v[116:119], v[104:107], v[26:29]
	v_mfma_f32_16x16x32_f16 v[30:33], v[120:123], v[104:107], v[30:33]
	v_mfma_f32_16x16x32_f16 v[34:37], v[124:127], v[104:107], v[34:37]
	v_mfma_f32_16x16x32_f16 v[38:41], v[128:131], v[104:107], v[38:41]
	v_mfma_f32_16x16x32_f16 v[42:45], v[132:135], v[104:107], v[42:45]
	v_mfma_f32_16x16x32_f16 v[46:49], v[136:139], v[104:107], v[46:49]
	s_waitcnt lgkmcnt(11)
	v_mfma_f32_16x16x32_f16 v[50:53], v[116:119], v[108:111], v[50:53]
	v_mfma_f32_16x16x32_f16 v[54:57], v[120:123], v[108:111], v[54:57]
	v_mfma_f32_16x16x32_f16 v[58:61], v[124:127], v[108:111], v[58:61]
	v_mfma_f32_16x16x32_f16 v[62:65], v[128:131], v[108:111], v[62:65]
	v_mfma_f32_16x16x32_f16 v[66:69], v[132:135], v[108:111], v[66:69]
	v_mfma_f32_16x16x32_f16 v[70:73], v[136:139], v[108:111], v[70:73]
	s_waitcnt lgkmcnt(10)
	v_mfma_f32_16x16x32_f16 v[74:77], v[116:119], v[112:115], v[74:77]
	v_mfma_f32_16x16x32_f16 v[78:81], v[120:123], v[112:115], v[78:81]
	v_mfma_f32_16x16x32_f16 v[82:85], v[124:127], v[112:115], v[82:85]
	v_mfma_f32_16x16x32_f16 v[86:89], v[128:131], v[112:115], v[86:89]
	v_mfma_f32_16x16x32_f16 v[90:93], v[132:135], v[112:115], v[90:93]
	v_mfma_f32_16x16x32_f16 v[94:97], v[136:139], v[112:115], v[94:97]
	s_waitcnt lgkmcnt(0)
	v_mfma_f32_16x16x32_f16 v[2:5], v[156:159], v[140:143], v[2:5]
	v_mfma_f32_16x16x32_f16 v[6:9], v[160:163], v[140:143], v[6:9]
	v_mfma_f32_16x16x32_f16 v[10:13], v[164:167], v[140:143], v[10:13]
	v_mfma_f32_16x16x32_f16 v[14:17], v[168:171], v[140:143], v[14:17]
	v_mfma_f32_16x16x32_f16 v[18:21], v[172:175], v[140:143], v[18:21]
	v_mfma_f32_16x16x32_f16 v[22:25], v[176:179], v[140:143], v[22:25]
	v_mfma_f32_16x16x32_f16 v[26:29], v[156:159], v[144:147], v[26:29]
	v_mfma_f32_16x16x32_f16 v[30:33], v[160:163], v[144:147], v[30:33]
	v_mfma_f32_16x16x32_f16 v[34:37], v[164:167], v[144:147], v[34:37]
	v_mfma_f32_16x16x32_f16 v[38:41], v[168:171], v[144:147], v[38:41]
	v_mfma_f32_16x16x32_f16 v[42:45], v[172:175], v[144:147], v[42:45]
	v_mfma_f32_16x16x32_f16 v[46:49], v[176:179], v[144:147], v[46:49]
	v_mfma_f32_16x16x32_f16 v[50:53], v[156:159], v[148:151], v[50:53]
	v_mfma_f32_16x16x32_f16 v[54:57], v[160:163], v[148:151], v[54:57]
	v_mfma_f32_16x16x32_f16 v[58:61], v[164:167], v[148:151], v[58:61]
	v_mfma_f32_16x16x32_f16 v[62:65], v[168:171], v[148:151], v[62:65]
	v_mfma_f32_16x16x32_f16 v[66:69], v[172:175], v[148:151], v[66:69]
	v_mfma_f32_16x16x32_f16 v[70:73], v[176:179], v[148:151], v[70:73]
	v_mfma_f32_16x16x32_f16 v[74:77], v[156:159], v[152:155], v[74:77]
	v_mfma_f32_16x16x32_f16 v[78:81], v[160:163], v[152:155], v[78:81]
	v_mfma_f32_16x16x32_f16 v[82:85], v[164:167], v[152:155], v[82:85]
	v_mfma_f32_16x16x32_f16 v[86:89], v[168:171], v[152:155], v[86:89]
	v_mfma_f32_16x16x32_f16 v[90:93], v[172:175], v[152:155], v[90:93]
	v_mfma_f32_16x16x32_f16 v[94:97], v[176:179], v[152:155], v[94:97]
	s_branch .LBB2_6
